# idle-time scheduling of the layer-1 weight conversion, both windows filled: 4096 items at the end of layer 0's down-projection phase, 4608 in layer 1's in-projection slack, 5760 left in layer 0's in-p
# speedup vs baseline: 1.0050x; 1.0027x over previous
; #define LAS __attribute__((address_space(3)))
; __device__ __forceinline__ int opaque_tid() { int t = threadIdx.x; asm volatile("" : "+v"(t)); return t; }
;     __device__ __forceinline__ bool next(int i, Unit& u) const {
;         const long L = (long)i * G + c; if (L >= nwg) return false;
;         int wgid = (int)L; { const int q = nwg / NXCD, r = nwg % NXCD, xcd = wgid % NXCD, off = wgid / NXCD; wgid = (xcd < r ? xcd * (q + 1) : r * (q + 1) + (xcd - r) * q) + off; }
;         const int nig = WGM * nN, gid = wgid / nig, fm = gid * WGM, gsz = (nM - fm) < WGM ? (nM - fm) : WGM;
;         u.pm = fm + ((wgid % nig) % gsz); u.pn = (wgid % nig) / gsz; u.e = 0; u.rows = 256;
;         u.a = A + (size_t)u.pm * tstepA; u.b = Bt + (size_t)u.pn * tstep; return true;
; __device__ __forceinline__ void pj_mfma(const Args& a, LAS unsigned char* lds, int layer) {
;     pg8::DenseOrder So; So.init(a.ws + WS_ACT, a.ws + WS_WIN + (size_t)layer * 3328 * D * 2, NTOK, 3328, D, gridDim.x, blockIdx.x);
;     LAS float* gl = (LAS float*)(lds + SEG_OFF + 256);
;     { const int t_ = opaque_tid(); if (t_ < 256) { const int w = t_ >> 6, i = t_ & 63; const float* gp_ = w == 0 ? a.in[I_QGF] : w == 1 ? a.in[I_KGF] : w == 2 ? a.in[I_QGD] : a.in[I_KGD]; gl[t_] = gp_[layer * 64 + i]; } }
;     __syncthreads();
;     EpiProj E{(bf16_t*)(a.ws + WS_PROJ), gl};
;     pg8::gemm_phase<EpiProj, pg8::DenseOrder>(lds, D, So, E);
;     if ((int)blockIdx.x >= (int)gridDim.x - 32) cumsum_unit(a, lds, blockIdx.x - (gridDim.x - 32));
;     if (layer + 1 < NL) { __syncthreads(); constexpr int I_SPLIT = 10240;
;         const int half = gridDim.x / 2; const bool upper = (int)blockIdx.x >= half;
;         p0_prep(a, lds, layer + 1, upper ? half : 0, upper ? (int)gridDim.x - half : half, upper ? 0 : I_SPLIT, upper ? I_SPLIT : (1 << 30)); }
.LBB0_101:
	s_or_b64 exec, exec, s[0:1]
	s_mov_b32 vcc_lo, 0
	s_nop 1
	v_writelane_b32 v254, vcc_lo, 60
	s_nop 1
	s_mov_b32 vcc_lo, 0
	s_nop 1
	v_writelane_b32 v254, vcc_lo, 62
	s_nop 1
	s_waitcnt lgkmcnt(0)
	s_barrier
	s_load_dwordx2 s[92:93], s[54:55], 0xa0
	s_load_dwordx16 s[12:27], s[54:55], 0x20
	s_load_dwordx4 s[0:3], s[54:55], 0x90
	s_movk_i32 s5, 0xd1
	s_mov_b32 s67, 0
	s_waitcnt vmcnt(0)
	v_mbcnt_lo_u32_b32 v1, -1, 0
	v_mbcnt_hi_u32_b32 v199, -1, v1
	s_waitcnt lgkmcnt(0)
	v_writelane_b32 v252, s0, 8
	v_and_b32_e32 v240, 64, v199
	s_mul_hi_u32 s85, s77, 0x600
	v_writelane_b32 v252, s1, 9
	v_writelane_b32 v252, s2, 10
	v_writelane_b32 v252, s3, 11
	s_add_u32 s0, s92, 0x100000
	s_addc_u32 s1, s93, 0
	v_writelane_b32 v252, s0, 12
	s_add_u32 s96, s92, 0xbc00000
	s_addc_u32 s97, s93, 0
	v_writelane_b32 v252, s1, 13
	s_lshl_b32 s0, s61, 3
	s_add_u32 s10, s92, 0x180000
	s_addc_u32 s11, s93, 0
	s_add_u32 s80, s92, 0x7c00000
	s_addc_u32 s81, s93, 0
	v_writelane_b32 v252, s0, 14
	s_add_u32 s0, s92, 0xfc00000
	s_addc_u32 s1, s93, 0
	s_add_u32 s50, s92, 0x18c00000
	s_addc_u32 s51, s93, 0
	s_add_u32 s2, s92, 0xa00000
	s_addc_u32 s3, s93, 0
	v_writelane_b32 v252, s2, 15
	s_cmpk_lt_i32 s61, 0x680
	s_mul_i32 s84, s77, 0x600
	v_writelane_b32 v252, s3, 16
	s_cselect_b64 s[2:3], -1, 0
	v_writelane_b32 v252, s2, 17
	v_mov_b32_e32 v35, 0
	v_add_u32_e32 v241, 64, v240
	v_writelane_b32 v252, s3, 18
	s_ashr_i32 s2, s61, 31
	v_writelane_b32 v252, s2, 19
	s_lshr_b32 s2, s2, 29
	s_add_i32 s3, s61, s2
	s_ashr_i32 s2, s3, 3
	s_and_b32 s3, s3, -8
	s_sub_i32 s3, s61, s3
	s_lshl_b32 s4, s3, 6
	s_cmp_lt_i32 s3, 0
	s_cselect_b32 s5, s5, 0xd0
	s_mul_i32 s5, s5, s3
	s_mulk_i32 s3, 0x41
	s_cselect_b32 s3, s3, s4
	s_add_i32 s5, s5, s2
	s_mul_hi_i32 s4, s5, 0x4ec4ec4f
	s_lshr_b32 s6, s4, 31
	s_ashr_i32 s4, s4, 5
	s_add_i32 s4, s4, s6
	s_mul_i32 s6, s4, 0x68
	s_sub_i32 s5, s5, s6
	s_lshl_b32 s7, s4, 3
	s_bfe_i32 s4, s5, 0x80000
	s_bfe_u32 s4, s4, 0x3000c
	s_add_i32 s6, s5, s4
	s_bfe_i32 s4, s6, 0x80000
	s_and_b32 s6, s6, 0xf8
	s_sub_i32 s5, s5, s6
	s_sext_i32_i16 s8, s4
	s_sext_i32_i8 s5, s5
	s_add_i32 s28, s7, s5
	s_ashr_i32 s5, s8, 3
	v_writelane_b32 v252, s5, 20
	s_mov_b32 s6, s28
	s_ashr_i32 s29, s28, 31
	v_writelane_b32 v252, s6, 21
	s_lshr_b32 s4, s8, 3
	v_xor_b32_e32 v236, 16, v199
	v_writelane_b32 v252, s7, 22
	s_lshl_b64 s[6:7], s[28:29], 19
	s_add_u32 s6, s80, s6
	s_addc_u32 s7, s81, s7
	v_writelane_b32 v252, s6, 23
	s_bfe_i64 s[4:5], s[4:5], 0x100000
	s_lshl_b64 s[4:5], s[4:5], 19
	v_writelane_b32 v252, s7, 24
	v_writelane_b32 v252, s4, 25
	v_xor_b32_e32 v237, 32, v199
	v_mov_b32_e32 v238, 1
	v_writelane_b32 v252, s5, 26
	s_ashr_i32 s4, s77, 31
	v_writelane_b32 v252, s4, 27
	s_sub_i32 s4, s77, 32
	s_cmp_ge_i32 s61, s4
	s_cselect_b64 s[6:7], -1, 0
	v_writelane_b32 v252, s6, 28
	s_sub_i32 s4, s61, s4
	s_and_b32 s5, s4, 3
	v_writelane_b32 v252, s7, 29
	s_ashr_i32 s6, s4, 2
	s_ashr_i32 s7, s6, 31
	s_lshl_b32 s5, s5, 2
	s_add_u32 s5, s10, s5
	v_writelane_b32 v252, s10, 30
	s_addc_u32 s8, s11, 0
	s_lshl_b64 s[6:7], s[6:7], 16
	s_add_u32 s6, s5, s6
	s_addc_u32 s7, s8, s7
	s_add_u32 s28, s92, 0x200000
	s_addc_u32 s29, s93, 0
	s_ashr_i32 s5, s4, 31
	s_lshl_b64 s[4:5], s[4:5], 14
	v_writelane_b32 v252, s11, 31
	s_add_u32 s4, s28, s4
	v_writelane_b32 v252, s6, 32
	s_addc_u32 s5, s29, s5
	s_lshr_b32 s8, s77, 1
	v_writelane_b32 v252, s7, 33
	s_sub_i32 s9, s77, s8
	v_writelane_b32 v252, s4, 34
	s_cmp_lt_i32 s61, s8
	v_mov_b32_e32 v198, 0x358637bd
	v_writelane_b32 v252, s5, 35
	s_cselect_b64 s[4:5], -1, 0
	s_and_b64 s[6:7], s[4:5], exec
	s_cselect_b32 s6, s8, s9
	s_movk_i32 s7, 0x1680
	s_cselect_b32 s10, 0, s8
	s_cselect_b32 s8, 0x14c8, 0
	s_cselect_b32 s7, s7, 0x14c8
	s_lshl_b32 s6, s6, 3
	v_writelane_b32 v252, s7, 36
	s_cmp_ge_i32 s61, s10
	v_writelane_b32 v252, s6, 37
	s_cselect_b64 s[6:7], -1, 0
	s_or_b64 s[4:5], s[36:37], s[4:5]
	s_load_dwordx8 s[36:43], s[54:55], 0x60
	s_and_b64 s[4:5], s[6:7], s[4:5]
	v_writelane_b32 v252, s4, 38
	v_mov_b32_e32 v201, 1.0
	v_mov_b32_e32 v239, 0x7f800000
	v_writelane_b32 v252, s5, 39
	s_sub_i32 s4, s61, s10
	s_lshl_b32 s4, s4, 3
	s_add_i32 s4, s4, s8
	s_waitcnt lgkmcnt(0)
	s_mov_b64 s[8:9], s[40:41]
	v_writelane_b32 v252, s4, 40
	s_add_u32 s6, s38, 0x400000
	s_mov_b64 s[10:11], s[42:43]
	s_mov_b64 s[4:5], s[36:37]
	v_writelane_b32 v252, s4, 41
	v_mov_b32_e32 v202, 0x3f317218
	v_mov_b32_e32 v242, 0xff800000
	v_writelane_b32 v252, s5, 42
	v_writelane_b32 v252, s6, 43
	v_writelane_b32 v252, s7, 44
	v_writelane_b32 v252, s8, 45
	v_writelane_b32 v252, s9, 46
	v_writelane_b32 v252, s10, 47
	v_writelane_b32 v252, s11, 48
	s_addc_u32 s7, s39, 0
	v_writelane_b32 v252, s6, 49
	s_add_u32 s4, s16, 0xd04000
	s_movk_i32 s74, 0x1ff
	v_writelane_b32 v252, s7, 50
	v_writelane_b32 v252, s12, 51
	s_addc_u32 s5, s17, 0
	s_mov_b32 s76, 0x800000
	v_writelane_b32 v255, s25, 0
	v_writelane_b32 v255, s26, 1
	v_writelane_b32 v255, s27, 2
	v_writelane_b32 v255, s4, 3
	v_writelane_b32 v252, s13, 52
	v_writelane_b32 v252, s14, 53
	v_writelane_b32 v255, s5, 4
	s_add_u32 s4, s92, 0x5b00000
	s_addc_u32 s5, s93, 0
	v_writelane_b32 v255, s4, 5
	v_writelane_b32 v252, s15, 54
	v_writelane_b32 v252, s16, 55
	v_writelane_b32 v255, s5, 6
	s_add_u32 s4, s92, 0x1b00000
	s_addc_u32 s5, s93, 0
	s_add_u32 s82, s92, 0x700000
	v_writelane_b32 v255, s4, 7
	s_addc_u32 s83, s93, 0
	v_writelane_b32 v252, s17, 56
	v_writelane_b32 v255, s5, 8
	s_add_u32 s4, s92, 0x14000
	v_writelane_b32 v255, s4, 9
	s_addc_u32 s4, s93, 0
	s_add_i32 s6, s61, 0x900
	s_cmpk_lt_i32 s61, 0x200
	v_writelane_b32 v255, s4, 10
	s_cselect_b64 s[4:5], -1, 0
	v_writelane_b32 v255, s4, 11
	v_writelane_b32 v252, s18, 57
;     ...
;         if (u < AT_NFOX) {
;             const int qb = 15 - (u >> 5), bh = u & 31, b = bh >> 2, h = bh & 3, q0 = qb * 256;
;             const size_t rb = (size_t)b * S;
;             const bf16_t* Kb = proj + ((size_t)(4 + h) * NTOK + rb) * 64;
;             const bf16_t* Vb = proj + ((size_t)(8 + h) * NTOK + rb) * 64;
;             const float* cum = cumall + (size_t)bh * S;
;             const int jhi = 4 * qb + 3;
;             fox_cr = cum[q0]; fox_cv = cum[64 * (lane <= jhi ? lane : jhi) + 63]; fox_cq = cum[q0 + 32 * wid + r32];
;             if (!(dbg & 1)) { FOX_ISSUE(0); FOX_ISSUE(1); FOX_ISSUE(2); }
;             const bf16_t* Q = proj + ((size_t)(0 + h) * NTOK + rb + q0 + 32 * wid + r32) * 64;
; #pragma unroll
;             for (int d0 = 0; d0 < 4; ++d0) qr[d0] = *(const bf16x8*)(Q + d0 * 16 + hi * 8);
;         } else if (u < AT_NFOX + AT_NDIL) {
;             const int v2 = u - AT_NFOX, bh = v2 % 48, rest = v2 / 48, b = bh / 6, h = bh % 6, p = rest >> 4, x = rest & 15;
;             const int dil = p == 0 ? 1 : p == 1 ? 4 : 16, res = x % dil, nb2 = x / dil;
;             const size_t rb = (size_t)b * S;
;             const bf16_t* Kb = proj + ((size_t)(22 + h) * NTOK + rb) * 64;
;             const bf16_t* Vb = proj + ((size_t)(28 + h) * NTOK + rb) * 64;
;             const int mk_base = 256 * nb2 - 128, tt_lo = nb2 == 0 ? 2 : 0;
;             const size_t rs = (size_t)64 * dil;
; #pragma unroll
;     ...
;             if (tid < 256) { const int st = tid - 64; tab[tid] = (st >= 0 && st <= 128) ? relb[t5_bucket(st * dil) * 6 + h] : -INFINITY; }
;             const size_t trow = (size_t)(256 * nb2 + 32 * wid + r32) * dil + res;
;             const bf16_t* Q = proj + ((size_t)(16 + h) * NTOK + rb + trow) * 64;
; #pragma unroll
;             for (int d0 = 0; d0 < 4; ++d0) qr[d0] = *(const bf16x8*)(Q + d0 * 16 + hi * 8);
;         } else {
;             const int v2 = u - AT_NFOX - AT_NDIL, qb = 15 - v2 / 48, bh = v2 % 48, b = bh / 6, h = bh % 6, q0 = qb * 256;
;             const size_t rb = (size_t)b * S;
;             const bf16_t* Kb = proj + ((size_t)(40 + h) * NTOK + rb) * 64;
;             const bf16_t* Vb = proj + ((size_t)(46 + h) * NTOK + rb) * 64;
;             const int jhi = (q0 + 254) >> 6;
;             if (!(dbg & 1)) { SB_ISSUE(0); SB_ISSUE(1); SB_ISSUE(2); }
	v_writelane_b32 v252, s19, 58
	v_writelane_b32 v255, s5, 12
	s_and_b64 s[4:5], s[4:5], exec
	s_cselect_b32 s13, s61, s6
	s_cmpk_lt_i32 s13, 0xe00
	s_cselect_b64 s[4:5], -1, 0
	v_writelane_b32 v255, s4, 13
	s_cmpk_gt_i32 s13, 0x1ff
	s_mov_b32 s17, s67
	v_writelane_b32 v255, s5, 14
	s_cselect_b64 s[4:5], -1, 0
	v_writelane_b32 v255, s4, 15
	s_cmpk_gt_u32 s13, 0xaff
	v_writelane_b32 v252, s20, 59
	v_writelane_b32 v255, s5, 16
	s_cselect_b64 s[4:5], -1, 0
	v_writelane_b32 v255, s4, 17
	v_writelane_b32 v252, s21, 60
	s_mov_b32 s21, s67
	v_writelane_b32 v255, s5, 18
	s_add_i32 s4, s13, 0xf500
	s_and_b32 s5, s4, 0xffff
	s_mul_i32 s5, s5, 0xaaab
	s_lshr_b32 s5, s5, 21
	s_mul_i32 s6, s5, 48
	s_sub_i32 s4, s4, s6
	s_and_b32 s6, s4, 0xff
	s_mulk_i32 s6, 0xab
	s_bfe_u32 s6, s6, 0x6000a
	s_mul_i32 s7, s6, 6
	s_sub_i32 s4, s4, s7
	s_and_b32 s4, s4, 0xff
	s_lshl_b32 s6, s6, 12
	s_lshl_b32 s4, s4, 15
	s_add_i32 s7, s6, s4
	s_lshl_b32 s7, s7, 7
	s_add_i32 s8, s7, 0xb800000
	s_add_u32 s8, s96, s8
	s_addc_u32 s9, s97, 0
	s_add_i32 s7, s7, 0xa000000
	s_add_u32 s7, s96, s7
	s_addc_u32 s10, s97, 0
	s_lshl_b32 s11, s5, 14
	s_sub_i32 s12, 0x3f000, s11
	s_lshl_b32 s12, s12, 1
	s_add_u32 s14, s7, s12
	s_addc_u32 s15, s10, 0
	v_writelane_b32 v255, s14, 19
	v_writelane_b32 v252, s22, 61
	v_writelane_b32 v252, s23, 62
	v_writelane_b32 v255, s15, 20
	s_add_u32 s14, s8, s12
	s_addc_u32 s15, s9, 0
	s_sub_i32 s12, 0x3e000, s11
	v_writelane_b32 v255, s14, 21
	s_lshl_b32 s12, s12, 1
	v_writelane_b32 v252, s24, 63
	v_writelane_b32 v255, s15, 22
	s_add_u32 s14, s7, s12
	s_addc_u32 s15, s10, 0
	v_writelane_b32 v255, s14, 23
	s_movk_i32 s56, 0x7f
	s_mov_b32 s57, 0xff800000
	v_writelane_b32 v255, s15, 24
	s_add_u32 s14, s8, s12
	s_addc_u32 s15, s9, 0
	s_sub_i32 s11, 0x3d000, s11
	v_writelane_b32 v255, s14, 25
	s_lshl_b32 s11, s11, 1
	s_mov_b32 s65, 0xc2ce8ed0
	v_writelane_b32 v255, s15, 26
	s_add_u32 s14, s7, s11
	s_addc_u32 s15, s10, 0
	s_add_u32 s8, s8, s11
	s_addc_u32 s9, s9, 0
	s_lshl_b32 s5, s5, 8
	s_sub_i32 s4, s4, s5
	s_add_i32 s5, s13, 0xfe00
	s_add_i32 s4, s4, s6
	s_and_b32 s6, s5, 0xffff
	s_mul_i32 s6, s6, 0xaaab
	s_lshr_b32 s7, s6, 21
	s_mul_i32 s7, s7, 48
	s_sub_i32 s5, s5, s7
	v_writelane_b32 v255, s14, 27
	s_and_b32 s7, s5, 0xff
	s_mulk_i32 s7, 0xab
	v_writelane_b32 v255, s15, 28
	v_writelane_b32 v255, s8, 29
	s_bfe_u32 s7, s7, 0x6000a
	s_add_i32 s4, s4, 0x110f00
	v_writelane_b32 v255, s9, 30
	s_mul_i32 s8, s7, 6
	s_sub_i32 s5, s5, s8
	s_and_b32 s5, s5, 0xff
	s_lshl_b32 s7, s7, 12
	s_lshl_b32 s8, s5, 15
	s_add_i32 s7, s7, s8
	v_writelane_b32 v255, s4, 31
	s_bfe_u32 s4, s6, 0x40015
	s_lshl_b32 s6, s7, 7
	s_add_u32 s6, s96, s6
	s_addc_u32 s8, s97, 0
	s_add_u32 s9, s6, 0x5800000
	s_addc_u32 s10, s8, 0
	s_add_u32 s6, s6, 0x7000000
	s_addc_u32 s8, s8, 0
	s_lshl_b32 s11, s4, 7
	s_or_b32 s12, s11, 0x60000
	s_add_u32 s14, s9, s12
	s_addc_u32 s15, s10, 0
	v_writelane_b32 v255, s14, 32
	s_mov_b64 s[44:45], -1
	s_mov_b64 s[86:87], 0x800
	v_writelane_b32 v255, s15, 33
	s_add_u32 s14, s6, s12
	s_addc_u32 s15, s8, 0
	v_writelane_b32 v255, s14, 34
	s_or_b32 s12, s11, 0x40000
	s_mov_b32 s60, 0xbfb8aa3b
	v_writelane_b32 v255, s15, 35
	s_add_u32 s14, s9, s12
	s_addc_u32 s15, s10, 0
	v_writelane_b32 v255, s14, 36
	s_mov_b64 s[88:89], 0x80
	s_mov_b64 s[94:95], 0x100
	v_writelane_b32 v255, s15, 37
	s_add_u32 s14, s6, s12
	s_addc_u32 s15, s8, 0
	v_writelane_b32 v255, s14, 38
	s_or_b32 s12, s11, 0x20000
	s_mov_b32 s62, s67
	v_writelane_b32 v255, s15, 39
	s_add_u32 s14, s9, s12
	s_addc_u32 s15, s10, 0
	v_writelane_b32 v255, s14, 40
	s_nop 1
	v_writelane_b32 v255, s15, 41
	s_add_u32 s14, s6, s12
	s_addc_u32 s15, s8, 0
	v_writelane_b32 v255, s14, 42
	s_nop 1
	v_writelane_b32 v255, s15, 43
	s_add_u32 s14, s9, s11
	s_addc_u32 s15, s10, 0
	v_writelane_b32 v255, s14, 44
	s_add_u32 s10, s6, s11
	s_addc_u32 s11, s8, 0
	v_writelane_b32 v255, s15, 45
	s_lshl_b32 s5, s5, 2
	v_writelane_b32 v255, s10, 46
	s_add_i32 s5, s5, 0
	s_add_i32 s5, s5, 0x21f00
	v_writelane_b32 v255, s11, 47
	v_writelane_b32 v255, s5, 48
	s_ashr_i32 s5, s13, 5
	s_or_b32 s4, s7, s4
	s_sub_i32 s5, 15, s5
	s_lshl_b32 s6, s13, 10
	s_and_b32 s7, s13, 31
	s_and_b32 s6, s6, 0x7000
	s_lshl_b32 s7, s7, 14
	s_or_b32 s14, s4, 0x80000
	s_and_b32 s8, s13, 3
	s_lshl_b32 s16, s5, 8
	s_add_u32 s18, s28, s7
	s_addc_u32 s19, s29, 0
	s_lshl_b32 s7, s5, 2
	v_writelane_b32 v255, s13, 49
	s_or_b32 s20, s7, 3
	s_lshl_b64 s[4:5], s[16:17], 2
	v_writelane_b32 v255, s28, 50
	s_add_u32 s4, s18, s4
	v_writelane_b32 v255, s29, 51
	s_addc_u32 s5, s19, s5
	v_writelane_b32 v255, s4, 52
	s_mov_b32 s15, s67
	s_nop 0
	v_writelane_b32 v255, s5, 53
	s_lshl_b32 s4, s8, 22
	s_lshl_b32 s5, s6, 7
	s_or_b32 s4, s5, s4
	s_add_u32 s4, s96, s4
	s_addc_u32 s5, s97, 0
	s_add_u32 s9, s4, 0x2000000
	s_addc_u32 s10, s5, 0
	s_add_u32 s11, s4, 0x1000000
	s_addc_u32 s12, s5, 0
	s_lshl_b64 s[4:5], s[20:21], 13
	s_add_u32 s22, s11, s4
	s_addc_u32 s23, s12, s5
	v_writelane_b32 v255, s22, 54
	s_add_u32 s4, s9, s4
	s_addc_u32 s5, s10, s5
	v_writelane_b32 v255, s23, 55
	v_writelane_b32 v255, s4, 56
	s_lshl_b32 s66, s20, 6
	s_nop 0
	v_writelane_b32 v255, s5, 57
	s_mov_b32 s4, s20
	v_writelane_b32 v255, s4, 58
	s_nop 1
	v_writelane_b32 v255, s5, 59
	s_lshl_b64 s[4:5], s[66:67], 2
	s_add_u32 s4, s18, s4
	s_addc_u32 s5, s19, s5
; #define LAS __attribute__((address_space(3)))
; #define FOX_ISSUE(i) do { const int j_ = jhi - (i), bf_ = (i) & 3; dma_kv(lds, bf_, Kb + (size_t)j_ * 4096, Vb + (size_t)j_ * 4096, 64, wid, lane); \
;         glds4(cum + j_ * 64 + lane, (unsigned)__builtin_amdgcn_readfirstlane(l0 + L_CK + bf_ * 256)); } while (0)
;     ...
;     bf16x8 qr[4];
;     float fox_cr = 0.f, fox_cv = 0.f, fox_cq = 0.f;
;     auto prologue = [&](int u) {
;         if (!UNIT_ON(u)) return;
;         int lane = tid & 63; asm volatile("" : "+v"(lane));
;         const int r32 = lane & 31, hi = lane >> 5;
;         if (u < AT_NFOX) {
;             const int qb = 15 - (u >> 5), bh = u & 31, b = bh >> 2, h = bh & 3, q0 = qb * 256;
;             const size_t rb = (size_t)b * S;
;             const bf16_t* Kb = proj + ((size_t)(4 + h) * NTOK + rb) * 64;
;             const bf16_t* Vb = proj + ((size_t)(8 + h) * NTOK + rb) * 64;
;             const float* cum = cumall + (size_t)bh * S;
;             const int jhi = 4 * qb + 3;
;             fox_cr = cum[q0]; fox_cv = cum[64 * (lane <= jhi ? lane : jhi) + 63]; fox_cq = cum[q0 + 32 * wid + r32];
;             if (!(dbg & 1)) { FOX_ISSUE(0); FOX_ISSUE(1); FOX_ISSUE(2); }
;             const bf16_t* Q = proj + ((size_t)(0 + h) * NTOK + rb + q0 + 32 * wid + r32) * 64;
; #pragma unroll
;             for (int d0 = 0; d0 < 4; ++d0) qr[d0] = *(const bf16x8*)(Q + d0 * 16 + hi * 8);
; __device__ __forceinline__ void op_mfma(const Args& a, LAS unsigned char* lds, int layer, bf16_t* outp = nullptr) {
;     pg8::DenseOrder So; So.init(a.ws + WS_ACT, a.ws + WS_WOUT + (size_t)layer * D * D * 2, NTOK, D, D, gridDim.x, blockIdx.x, (size_t)256 * 128);
;     bf16_t* xb = (bf16_t*)(a.ws + WS_XB);
;     EpiOut E{layer == 0 ? a.in[I_X] : nullptr, xb, outp ? outp : xb, (const float*)(a.ws + WS_MOD) + (size_t)layer * NB * 6144 + 2048};
;     pg8::gemm_phase<EpiOut, pg8::DenseOrder>(lds, D, So, E, 128u, (size_t)NTOK * 128);
	v_writelane_b32 v255, s4, 60
	s_or_b32 s66, s7, 2
	s_nop 0
	v_writelane_b32 v255, s5, 61
	s_lshl_b64 s[4:5], s[66:67], 13
	s_add_u32 s20, s11, s4
	s_addc_u32 s21, s12, s5
	s_add_u32 s4, s9, s4
	s_addc_u32 s5, s10, s5
	v_writelane_b32 v253, s4, 0
	s_lshl_b32 s66, s66, 6
	v_writelane_b32 v255, s20, 62
	v_writelane_b32 v253, s5, 1
	s_lshl_b64 s[4:5], s[66:67], 2
	s_add_u32 s4, s18, s4
	s_addc_u32 s5, s19, s5
	v_writelane_b32 v253, s4, 2
	s_or_b32 s66, s7, 1
	v_writelane_b32 v255, s21, 63
	v_writelane_b32 v253, s5, 3
	s_lshl_b64 s[4:5], s[66:67], 13
	s_add_u32 s20, s11, s4
	s_addc_u32 s21, s12, s5
	v_writelane_b32 v253, s20, 4
	s_add_u32 s4, s9, s4
	s_addc_u32 s5, s10, s5
	v_writelane_b32 v253, s21, 5
	v_writelane_b32 v253, s4, 6
	s_lshl_b32 s66, s66, 6
	s_mov_b32 s9, s67
	v_writelane_b32 v253, s5, 7
	s_lshl_b64 s[4:5], s[66:67], 2
	s_add_u32 s4, s18, s4
	v_writelane_b32 v253, s18, 8
	s_addc_u32 s5, s19, s5
	s_nop 0
	v_writelane_b32 v253, s19, 9
	v_writelane_b32 v253, s4, 10
	s_nop 1
	v_writelane_b32 v253, s5, 11
	s_lshl_b32 s4, s8, 15
	s_or_b32 s4, s6, s4
	s_mov_b32 s6, s16
	v_writelane_b32 v253, s6, 12
	s_add_i32 s4, s4, s16
	s_mov_b32 s8, s77
	v_writelane_b32 v253, s7, 13
	s_mov_b32 s6, s61
	s_mov_b32 s7, s67
	v_writelane_b32 v253, s4, 14
	s_lshl_b64 s[4:5], s[6:7], 9
	s_lshl_b64 s[70:71], s[8:9], 9
	v_writelane_b32 v253, s4, 15
	s_nop 1
	v_writelane_b32 v253, s5, 16
	s_add_u32 s4, s92, 0x8c00000
	s_addc_u32 s5, s93, 0
	v_writelane_b32 v253, s4, 17
	s_nop 1
	v_writelane_b32 v253, s5, 18
	s_add_u32 s4, s92, 0x1700000
	v_writelane_b32 v253, s4, 19
	s_addc_u32 s4, s93, 0
	v_writelane_b32 v253, s4, 20
	s_add_u32 s4, s92, 0x10000
	v_writelane_b32 v253, s4, 21
	s_addc_u32 s4, s93, 0
	v_writelane_b32 v253, s4, 22
	s_add_u32 s4, s92, 0x300000
	s_addc_u32 s5, s93, 0
	v_writelane_b32 v253, s4, 23
	s_nop 1
	v_writelane_b32 v253, s5, 24
	s_add_u32 s4, s92, 0x500000
	s_addc_u32 s5, s93, 0
	v_writelane_b32 v253, s4, 25
	s_cmpk_lt_i32 s61, 0x100
	s_nop 0
	v_writelane_b32 v253, s5, 26
	s_cselect_b64 s[4:5], -1, 0
	v_writelane_b32 v253, s4, 27
	s_nop 1
	v_writelane_b32 v253, s5, 28
	s_add_u32 s4, s92, 0x14400000
	s_addc_u32 s5, s93, 0
	v_writelane_b32 v253, s4, 29
	s_nop 1
	v_writelane_b32 v253, s5, 30
	s_add_i32 s4, s77, s61
	v_writelane_b32 v253, s4, 31
	s_add_u32 s4, s92, 0x7c00080
	s_addc_u32 s5, s93, 0
	s_add_i32 s2, s3, s2
	s_ashr_i32 s3, s2, 31
	s_lshr_b32 s3, s3, 27
	v_writelane_b32 v253, s4, 32
	s_add_i32 s3, s2, s3
	s_nop 0
	v_writelane_b32 v253, s5, 33
	s_and_b32 s4, s3, 0xffe0
	s_sub_i32 s2, s2, s4
	s_bfe_i32 s4, s2, 0x80000
	s_bfe_u32 s4, s4, 0x3000c
	s_add_i32 s4, s2, s4
	s_and_b32 s5, s4, 0xf8
	s_sub_i32 s2, s2, s5
	s_ashr_i32 s3, s3, 5
	s_bfe_i32 s4, s4, 0x80000
	s_lshl_b32 s3, s3, 3
	s_sext_i32_i16 s4, s4
	s_sext_i32_i8 s2, s2
	s_add_i32 s10, s3, s2
	s_ashr_i32 s2, s4, 3
	v_writelane_b32 v253, s2, 34
	s_lshr_b32 s2, s4, 3
	s_mov_b32 s4, s10
	s_ashr_i32 s11, s10, 31
	v_writelane_b32 v253, s4, 35
	s_nop 1
	v_writelane_b32 v253, s5, 36
	s_lshl_b64 s[4:5], s[10:11], 15
	s_add_u32 s4, s80, s4
	s_addc_u32 s5, s81, s5
	v_writelane_b32 v253, s14, 37
	s_bfe_i64 s[2:3], s[2:3], 0x100000
	s_lshl_b64 s[2:3], s[2:3], 19
	v_writelane_b32 v253, s15, 38
	v_writelane_b32 v253, s2, 39
	s_nop 1
	v_writelane_b32 v253, s3, 40
	s_add_u32 s2, s4, 0x4000
	s_addc_u32 s3, s5, 0
	v_writelane_b32 v253, s2, 41
	s_nop 1
	v_writelane_b32 v253, s3, 42
	s_add_u32 s2, s4, 0x400000
	v_writelane_b32 v253, s4, 43
	s_addc_u32 s3, s5, 0
	s_lshl_b64 s[52:53], s[8:9], 10
	v_writelane_b32 v253, s5, 44
	v_writelane_b32 v253, s2, 45
	s_add_i32 s64, 0, 0x13000
	s_nop 0
	v_writelane_b32 v253, s3, 46
	s_lshl_b32 s2, s61, 7
	v_writelane_b32 v253, s2, 47
	s_lshl_b32 s2, s77, 7
	v_writelane_b32 v253, s2, 48
	s_mul_i32 s2, s77, 0x3000
	v_writelane_b32 v253, s2, 49
	s_add_i32 s2, 0, 0x21c20
	v_writelane_b32 v253, s2, 50
	s_add_i32 s2, 0, 0x21c24
	v_writelane_b32 v253, s2, 51
	s_add_i32 s2, 0, 0x21000
	v_writelane_b32 v253, s2, 52
	s_add_i32 s2, 0, 0x21100
	v_writelane_b32 v253, s2, 53
	s_add_i32 s2, 0, 0x21200
	v_writelane_b32 v253, s2, 54
	s_add_i32 s2, 0, 0x21504
	v_writelane_b32 v253, s2, 55
	s_add_i32 s2, 0, 0x15040
	v_writelane_b32 v253, s2, 56
	s_add_i32 s2, 0, 0x15000
	v_writelane_b32 v253, s2, 57
	s_add_i32 s2, 0, 0x21e80
	v_writelane_b32 v253, s2, 58
	s_add_i32 s2, 0, 0x21e10
	v_writelane_b32 v253, s2, 59
	s_add_i32 s2, 0, 0x21e20
	v_writelane_b32 v253, s2, 60
	s_add_i32 s2, 0, 0x21e30
	v_writelane_b32 v253, s2, 61
	v_writelane_b32 v253, s54, 62
	s_load_dwordx2 s[4:5], s[54:55], 0x0
	s_mov_b32 s3, 0x42b17218
	v_writelane_b32 v253, s55, 63
	s_waitcnt lgkmcnt(0)
	v_writelane_b32 v254, s4, 0
	s_nop 1
	v_writelane_b32 v254, s5, 1
	s_lshl_b64 s[4:5], s[8:9], 13
	v_writelane_b32 v254, s4, 2
	s_nop 1
	v_writelane_b32 v254, s5, 3
	v_writelane_b32 v254, s6, 4
	s_lshl_b64 s[4:5], s[6:7], 12
	s_nop 0
	v_writelane_b32 v254, s7, 5
	v_writelane_b32 v254, s4, 6
	s_nop 1
	v_writelane_b32 v254, s5, 7
	s_lshl_b64 s[4:5], s[8:9], 14
	v_writelane_b32 v254, s4, 8
	s_nop 1
	v_writelane_b32 v254, s5, 9
	v_writelane_b32 v254, s8, 10
	s_lshl_b64 s[4:5], s[8:9], 12
	s_nop 0
	v_writelane_b32 v254, s9, 11
	v_writelane_b32 v254, s4, 12
	s_nop 1
	v_writelane_b32 v254, s5, 13
	v_writelane_b32 v254, s82, 14
	s_nop 1
	v_writelane_b32 v254, s83, 15
	s_branch .LBB0_104

; #define LAS __attribute__((address_space(3)))
; __device__ __forceinline__ int opaque_tid() { int t = threadIdx.x; asm volatile("" : "+v"(t)); return t; }
;     const int tid = opaque_tid(), lane = tid & 63, wave = tid >> 6;
;     LAS float* scr = (LAS float*)(lds + 49152) + wave * (64 * 33);
;     const int gw = ((int)blockIdx.x - blk0) * NWAVES + wave, ngw = nblk * NWAVES;
;     constexpr int I_L = 16 * 104 + 16 * 32 + 16 * 16 * 32 + 16 * 8 * 32;
;     if ((int)blockIdx.x < blk0 || (int)blockIdx.x >= blk0 + nblk) return;
;     float tv[32];
;     const int I_E = it_hi < I_L ? it_hi : I_L;
;     int it = it_lo + gw;
; __device__ __forceinline__ void pj_mfma(const Args& a, LAS unsigned char* lds, int layer) {
;     ...
;     if (layer + 1 < NL) { __syncthreads(); constexpr int I_SPLIT = 10240;
;         const int half = gridDim.x / 2; const bool upper = (int)blockIdx.x >= half;
;         p0_prep(a, lds, layer + 1, upper ? half : 0, upper ? (int)gridDim.x - half : half, upper ? 0 : I_SPLIT, upper ? I_SPLIT : (1 << 30)); }
.Lpj_l1_prep:
	s_lshr_b32 s4, s77, 1
	s_sub_i32 s5, s77, s4
	s_cmp_ge_u32 s61, s4
	s_cselect_b64 s[6:7], -1, 0
	s_sub_i32 s8, s61, s4
	s_lshl_b32 s8, s8, 3
	s_addk_i32 s8, 0x1680
	s_lshl_b32 s5, s5, 3
	s_movk_i32 s9, 0x2880
	s_nop 0
	v_writelane_b32 v252, s9, 36
	v_writelane_b32 v252, s5, 37
	v_writelane_b32 v252, s6, 38
	v_writelane_b32 v252, s7, 39
	v_writelane_b32 v252, s8, 40
	s_branch .Lprep_go
